# speedup vs baseline: 1.0414x; 1.0131x over previous
.Ltile0:
	s_mov_b32 s34, 0
	s_waitcnt vmcnt(5)
	s_waitcnt lgkmcnt(0)
	s_barrier
	s_mul_i32 s35, s33, 0xa000
	v_add_u32_e32 v240, s35, v222
	v_add_u32_e32 v241, s35, v223
	v_add_u32_e32 v242, s35, v224
	s_add_u32 s33, s33, 1
	s_cmp_eq_u32 s33, 3
	s_cselect_b32 s33, 0, s33
	ds_read_b128 v[244:247], v240 offset:6144
	ds_read_b128 v[252:255], v240 offset:7168
	v_mfma_scale_f32_16x16x128_f8f6f4 v[0:3], v[128:131], v[160:165], 0, v208, v216 op_sel_hi:[0,0,0] cbsz:4 blgp:2
	s_cmp_eq_u32 s34, 13
	s_cselect_b32 s36, s38, s36
	s_cselect_b32 s37, s39, s37
	s_mov_b32 m0, s40
	v_mfma_scale_f32_16x16x128_f8f6f4 v[16:19], v[132:135], v[160:165], 0, v209, v216 op_sel_hi:[0,0,0] cbsz:4 blgp:2
	ds_read_b128 v[184:187], v241 offset:0
	v_mfma_scale_f32_16x16x128_f8f6f4 v[20:23], v[132:135], v[166:171], 0, v209, v217 op_sel_hi:[0,0,0] cbsz:4 blgp:2
	buffer_load_dwordx4 v221, s[4:7], s36 offen lds
	v_mfma_scale_f32_16x16x128_f8f6f4 v[4:7], v[128:131], v[166:171], 0, v208, v217 op_sel_hi:[0,0,0] cbsz:4 blgp:2
	s_add_u32 m0, s40, 0x2000
	ds_read_b64 v[188:189], v242 offset:0
	v_mfma_scale_f32_16x16x128_f8f6f4 v[8:11], v[128:131], v[172:177], 0, v208, v218 op_sel_hi:[0,0,0] cbsz:4 blgp:2
	buffer_load_dwordx4 v225, s[4:7], s36 offen lds
	v_mfma_scale_f32_16x16x128_f8f6f4 v[24:27], v[132:135], v[172:177], 0, v209, v218 op_sel_hi:[0,0,0] cbsz:4 blgp:2
	s_add_u32 m0, s40, 0x4000
	ds_read_b128 v[190:193], v241 offset:1536
	v_mfma_scale_f32_16x16x128_f8f6f4 v[28:31], v[132:135], v[178:183], 0, v209, v219 op_sel_hi:[0,0,0] cbsz:4 blgp:2
	buffer_load_dwordx4 v221, s[4:7], s37 offen lds
	v_mfma_scale_f32_16x16x128_f8f6f4 v[12:15], v[128:131], v[178:183], 0, v208, v219 op_sel_hi:[0,0,0] cbsz:4 blgp:2
	s_add_u32 m0, s40, 0x6000
	ds_read_b64 v[194:195], v242 offset:1536
	v_mfma_scale_f32_16x16x128_f8f6f4 v[44:47], v[136:139], v[178:183], 0, v210, v219 op_sel_hi:[0,0,0] cbsz:4 blgp:2
	buffer_load_dwordx4 v225, s[4:7], s37 offen lds
	v_mfma_scale_f32_16x16x128_f8f6f4 v[60:63], v[140:143], v[178:183], 0, v211, v219 op_sel_hi:[0,0,0] cbsz:4 blgp:2
	s_add_u32 m0, s40, 0x8000
	ds_read_b128 v[196:199], v241 offset:3072
	v_mfma_scale_f32_16x16x128_f8f6f4 v[56:59], v[140:143], v[172:177], 0, v211, v218 op_sel_hi:[0,0,0] cbsz:4 blgp:2
	buffer_load_dwordx4 v226, s[4:7], s37 offen lds
	v_mfma_scale_f32_16x16x128_f8f6f4 v[40:43], v[136:139], v[172:177], 0, v210, v218 op_sel_hi:[0,0,0] cbsz:4 blgp:2
	ds_read_b64 v[200:201], v242 offset:3072
	v_mfma_scale_f32_16x16x128_f8f6f4 v[36:39], v[136:139], v[166:171], 0, v210, v217 op_sel_hi:[0,0,0] cbsz:4 blgp:2
	ds_read_b128 v[202:205], v241 offset:4608
	v_mfma_scale_f32_16x16x128_f8f6f4 v[52:55], v[140:143], v[166:171], 0, v211, v217 op_sel_hi:[0,0,0] cbsz:4 blgp:2
	ds_read_b64 v[206:207], v242 offset:4608
	v_mfma_scale_f32_16x16x128_f8f6f4 v[48:51], v[140:143], v[160:165], 0, v211, v216 op_sel_hi:[0,0,0] cbsz:4 blgp:2
	s_add_u32 s36, s36, 0x4000
	s_add_u32 s37, s37, 0x6000
	s_add_u32 s40, s40, 0xa000
	s_sub_u32 s41, s40, 0x1e000
	v_mfma_scale_f32_16x16x128_f8f6f4 v[32:35], v[136:139], v[160:165], 0, v210, v216 op_sel_hi:[0,0,0] cbsz:4 blgp:2
	s_cmp_ge_u32 s40, s49
	s_cselect_b32 s40, s41, s40
	ds_read_b128 v[132:135], v240 offset:1024
	v_mfma_scale_f32_16x16x128_f8f6f4 v[64:67], v[144:147], v[160:165], 0, v212, v216 op_sel_hi:[0,0,0] cbsz:4 blgp:2
	ds_read_b128 v[128:131], v240 offset:0
	v_mfma_scale_f32_16x16x128_f8f6f4 v[80:83], v[148:151], v[160:165], 0, v213, v216 op_sel_hi:[0,0,0] cbsz:4 blgp:2
	ds_read_b128 v[140:143], v240 offset:3072
	v_mfma_scale_f32_16x16x128_f8f6f4 v[84:87], v[148:151], v[166:171], 0, v213, v217 op_sel_hi:[0,0,0] cbsz:4 blgp:2
	ds_read_b128 v[136:139], v240 offset:2048
	v_mfma_scale_f32_16x16x128_f8f6f4 v[68:71], v[144:147], v[166:171], 0, v212, v217 op_sel_hi:[0,0,0] cbsz:4 blgp:2
	v_mfma_scale_f32_16x16x128_f8f6f4 v[72:75], v[144:147], v[172:177], 0, v212, v218 op_sel_hi:[0,0,0] cbsz:4 blgp:2
	v_mfma_scale_f32_16x16x128_f8f6f4 v[88:91], v[148:151], v[172:177], 0, v213, v218 op_sel_hi:[0,0,0] cbsz:4 blgp:2
	v_mfma_scale_f32_16x16x128_f8f6f4 v[92:95], v[148:151], v[178:183], 0, v213, v219 op_sel_hi:[0,0,0] cbsz:4 blgp:2
	v_mfma_scale_f32_16x16x128_f8f6f4 v[76:79], v[144:147], v[178:183], 0, v212, v219 op_sel_hi:[0,0,0] cbsz:4 blgp:2
	ds_read_b128 v[148:151], v240 offset:5120
	v_mfma_scale_f32_16x16x128_f8f6f4 v[108:111], v[152:155], v[178:183], 0, v214, v219 op_sel_hi:[0,0,0] cbsz:4 blgp:2
	ds_read_b128 v[144:147], v240 offset:4096
	v_mfma_scale_f32_16x16x128_f8f6f4 v[124:127], v[156:159], v[178:183], 0, v215, v219 op_sel_hi:[0,0,0] cbsz:4 blgp:2
	v_mfma_scale_f32_16x16x128_f8f6f4 v[120:123], v[156:159], v[172:177], 0, v215, v218 op_sel_hi:[0,0,0] cbsz:4 blgp:2
	v_mfma_scale_f32_16x16x128_f8f6f4 v[104:107], v[152:155], v[172:177], 0, v214, v218 op_sel_hi:[0,0,0] cbsz:4 blgp:2
	v_mfma_scale_f32_16x16x128_f8f6f4 v[100:103], v[152:155], v[166:171], 0, v214, v217 op_sel_hi:[0,0,0] cbsz:4 blgp:2
	v_mfma_scale_f32_16x16x128_f8f6f4 v[116:119], v[156:159], v[166:171], 0, v215, v217 op_sel_hi:[0,0,0] cbsz:4 blgp:2
	v_mfma_scale_f32_16x16x128_f8f6f4 v[112:115], v[156:159], v[160:165], 0, v215, v216 op_sel_hi:[0,0,0] cbsz:4 blgp:2
	v_mfma_scale_f32_16x16x128_f8f6f4 v[96:99], v[152:155], v[160:165], 0, v214, v216 op_sel_hi:[0,0,0] cbsz:4 blgp:2
	s_add_u32 s34, s34, 1
	s_waitcnt vmcnt(5)
	s_waitcnt lgkmcnt(0)
	s_barrier
	s_mul_i32 s35, s33, 0xa000
	v_add_u32_e32 v240, s35, v222
	v_add_u32_e32 v241, s35, v223
	v_add_u32_e32 v242, s35, v224
	s_add_u32 s33, s33, 1
	s_cmp_eq_u32 s33, 3
	s_cselect_b32 s33, 0, s33
	ds_read_b128 v[152:155], v240 offset:6144
	ds_read_b128 v[156:159], v240 offset:7168
	v_mfma_scale_f32_16x16x128_f8f6f4 v[0:3], v[128:131], v[184:189], v[0:3], v208, v216 op_sel_hi:[0,0,0] cbsz:4 blgp:2
	s_cmp_eq_u32 s34, 13
	s_cselect_b32 s36, s38, s36
	s_cselect_b32 s37, s39, s37
	s_mov_b32 m0, s40
	v_mfma_scale_f32_16x16x128_f8f6f4 v[16:19], v[132:135], v[184:189], v[16:19], v209, v216 op_sel_hi:[0,0,0] cbsz:4 blgp:2
	ds_read_b128 v[160:163], v241 offset:0
	v_mfma_scale_f32_16x16x128_f8f6f4 v[20:23], v[132:135], v[190:195], v[20:23], v209, v217 op_sel_hi:[0,0,0] cbsz:4 blgp:2
	buffer_load_dwordx4 v221, s[4:7], s36 offen lds
	v_mfma_scale_f32_16x16x128_f8f6f4 v[4:7], v[128:131], v[190:195], v[4:7], v208, v217 op_sel_hi:[0,0,0] cbsz:4 blgp:2
	s_add_u32 m0, s40, 0x2000
	ds_read_b64 v[164:165], v242 offset:0
	v_mfma_scale_f32_16x16x128_f8f6f4 v[8:11], v[128:131], v[196:201], v[8:11], v208, v218 op_sel_hi:[0,0,0] cbsz:4 blgp:2
	buffer_load_dwordx4 v225, s[4:7], s36 offen lds
	v_mfma_scale_f32_16x16x128_f8f6f4 v[24:27], v[132:135], v[196:201], v[24:27], v209, v218 op_sel_hi:[0,0,0] cbsz:4 blgp:2
	s_add_u32 m0, s40, 0x4000
	ds_read_b128 v[166:169], v241 offset:1536
	v_mfma_scale_f32_16x16x128_f8f6f4 v[28:31], v[132:135], v[202:207], v[28:31], v209, v219 op_sel_hi:[0,0,0] cbsz:4 blgp:2
	buffer_load_dwordx4 v221, s[4:7], s37 offen lds
	v_mfma_scale_f32_16x16x128_f8f6f4 v[12:15], v[128:131], v[202:207], v[12:15], v208, v219 op_sel_hi:[0,0,0] cbsz:4 blgp:2
	s_add_u32 m0, s40, 0x6000
	ds_read_b64 v[170:171], v242 offset:1536
	v_mfma_scale_f32_16x16x128_f8f6f4 v[44:47], v[136:139], v[202:207], v[44:47], v210, v219 op_sel_hi:[0,0,0] cbsz:4 blgp:2
	buffer_load_dwordx4 v225, s[4:7], s37 offen lds
	v_mfma_scale_f32_16x16x128_f8f6f4 v[60:63], v[140:143], v[202:207], v[60:63], v211, v219 op_sel_hi:[0,0,0] cbsz:4 blgp:2
	s_add_u32 m0, s40, 0x8000
	ds_read_b128 v[172:175], v241 offset:3072
	v_mfma_scale_f32_16x16x128_f8f6f4 v[56:59], v[140:143], v[196:201], v[56:59], v211, v218 op_sel_hi:[0,0,0] cbsz:4 blgp:2
	buffer_load_dwordx4 v226, s[4:7], s37 offen lds
	v_mfma_scale_f32_16x16x128_f8f6f4 v[40:43], v[136:139], v[196:201], v[40:43], v210, v218 op_sel_hi:[0,0,0] cbsz:4 blgp:2
	ds_read_b64 v[176:177], v242 offset:3072
	v_mfma_scale_f32_16x16x128_f8f6f4 v[36:39], v[136:139], v[190:195], v[36:39], v210, v217 op_sel_hi:[0,0,0] cbsz:4 blgp:2
	ds_read_b128 v[178:181], v241 offset:4608
	v_mfma_scale_f32_16x16x128_f8f6f4 v[52:55], v[140:143], v[190:195], v[52:55], v211, v217 op_sel_hi:[0,0,0] cbsz:4 blgp:2
	ds_read_b64 v[182:183], v242 offset:4608
	v_mfma_scale_f32_16x16x128_f8f6f4 v[48:51], v[140:143], v[184:189], v[48:51], v211, v216 op_sel_hi:[0,0,0] cbsz:4 blgp:2
	s_add_u32 s36, s36, 0x4000
	s_add_u32 s37, s37, 0x6000
	s_add_u32 s40, s40, 0xa000
	s_sub_u32 s41, s40, 0x1e000
	v_mfma_scale_f32_16x16x128_f8f6f4 v[32:35], v[136:139], v[184:189], v[32:35], v210, v216 op_sel_hi:[0,0,0] cbsz:4 blgp:2
	s_cmp_ge_u32 s40, s49
	s_cselect_b32 s40, s41, s40
	ds_read_b128 v[132:135], v240 offset:1024
	v_mfma_scale_f32_16x16x128_f8f6f4 v[64:67], v[144:147], v[184:189], v[64:67], v212, v216 op_sel_hi:[0,0,0] cbsz:4 blgp:2
	ds_read_b128 v[128:131], v240 offset:0
	v_mfma_scale_f32_16x16x128_f8f6f4 v[80:83], v[148:151], v[184:189], v[80:83], v213, v216 op_sel_hi:[0,0,0] cbsz:4 blgp:2
	ds_read_b128 v[140:143], v240 offset:3072
	v_mfma_scale_f32_16x16x128_f8f6f4 v[84:87], v[148:151], v[190:195], v[84:87], v213, v217 op_sel_hi:[0,0,0] cbsz:4 blgp:2
	ds_read_b128 v[136:139], v240 offset:2048
	v_mfma_scale_f32_16x16x128_f8f6f4 v[68:71], v[144:147], v[190:195], v[68:71], v212, v217 op_sel_hi:[0,0,0] cbsz:4 blgp:2
	v_mfma_scale_f32_16x16x128_f8f6f4 v[72:75], v[144:147], v[196:201], v[72:75], v212, v218 op_sel_hi:[0,0,0] cbsz:4 blgp:2
	v_mfma_scale_f32_16x16x128_f8f6f4 v[88:91], v[148:151], v[196:201], v[88:91], v213, v218 op_sel_hi:[0,0,0] cbsz:4 blgp:2
	v_mfma_scale_f32_16x16x128_f8f6f4 v[92:95], v[148:151], v[202:207], v[92:95], v213, v219 op_sel_hi:[0,0,0] cbsz:4 blgp:2
	v_mfma_scale_f32_16x16x128_f8f6f4 v[76:79], v[144:147], v[202:207], v[76:79], v212, v219 op_sel_hi:[0,0,0] cbsz:4 blgp:2
	ds_read_b128 v[148:151], v240 offset:5120
	v_mfma_scale_f32_16x16x128_f8f6f4 v[108:111], v[244:247], v[202:207], v[108:111], v214, v219 op_sel_hi:[0,0,0] cbsz:4 blgp:2
	ds_read_b128 v[144:147], v240 offset:4096
	v_mfma_scale_f32_16x16x128_f8f6f4 v[124:127], v[252:255], v[202:207], v[124:127], v215, v219 op_sel_hi:[0,0,0] cbsz:4 blgp:2
	v_mfma_scale_f32_16x16x128_f8f6f4 v[120:123], v[252:255], v[196:201], v[120:123], v215, v218 op_sel_hi:[0,0,0] cbsz:4 blgp:2
	v_mfma_scale_f32_16x16x128_f8f6f4 v[104:107], v[244:247], v[196:201], v[104:107], v214, v218 op_sel_hi:[0,0,0] cbsz:4 blgp:2
	v_mfma_scale_f32_16x16x128_f8f6f4 v[100:103], v[244:247], v[190:195], v[100:103], v214, v217 op_sel_hi:[0,0,0] cbsz:4 blgp:2
	v_mfma_scale_f32_16x16x128_f8f6f4 v[116:119], v[252:255], v[190:195], v[116:119], v215, v217 op_sel_hi:[0,0,0] cbsz:4 blgp:2
	v_mfma_scale_f32_16x16x128_f8f6f4 v[112:115], v[252:255], v[184:189], v[112:115], v215, v216 op_sel_hi:[0,0,0] cbsz:4 blgp:2
	v_mfma_scale_f32_16x16x128_f8f6f4 v[96:99], v[244:247], v[184:189], v[96:99], v214, v216 op_sel_hi:[0,0,0] cbsz:4 blgp:2
	s_add_u32 s34, s34, 1
.Lkloop0:
	s_waitcnt vmcnt(5)
	s_waitcnt lgkmcnt(0)
	s_barrier
	s_mul_i32 s35, s33, 0xa000
	v_add_u32_e32 v240, s35, v222
	v_add_u32_e32 v241, s35, v223
	v_add_u32_e32 v242, s35, v224
	s_add_u32 s33, s33, 1
	s_cmp_eq_u32 s33, 3
	s_cselect_b32 s33, 0, s33
	ds_read_b128 v[244:247], v240 offset:6144
	ds_read_b128 v[252:255], v240 offset:7168
	v_mfma_scale_f32_16x16x128_f8f6f4 v[0:3], v[128:131], v[160:165], v[0:3], v208, v216 op_sel_hi:[0,0,0] cbsz:4 blgp:2
	s_cmp_eq_u32 s34, 13
	s_cselect_b32 s36, s38, s36
	s_cselect_b32 s37, s39, s37
	s_mov_b32 m0, s40
	v_mfma_scale_f32_16x16x128_f8f6f4 v[16:19], v[132:135], v[160:165], v[16:19], v209, v216 op_sel_hi:[0,0,0] cbsz:4 blgp:2
	ds_read_b128 v[184:187], v241 offset:0
	v_mfma_scale_f32_16x16x128_f8f6f4 v[20:23], v[132:135], v[166:171], v[20:23], v209, v217 op_sel_hi:[0,0,0] cbsz:4 blgp:2
	buffer_load_dwordx4 v221, s[4:7], s36 offen lds
	v_mfma_scale_f32_16x16x128_f8f6f4 v[4:7], v[128:131], v[166:171], v[4:7], v208, v217 op_sel_hi:[0,0,0] cbsz:4 blgp:2
	s_add_u32 m0, s40, 0x2000
	ds_read_b64 v[188:189], v242 offset:0
	v_mfma_scale_f32_16x16x128_f8f6f4 v[8:11], v[128:131], v[172:177], v[8:11], v208, v218 op_sel_hi:[0,0,0] cbsz:4 blgp:2
	buffer_load_dwordx4 v225, s[4:7], s36 offen lds
	v_mfma_scale_f32_16x16x128_f8f6f4 v[24:27], v[132:135], v[172:177], v[24:27], v209, v218 op_sel_hi:[0,0,0] cbsz:4 blgp:2
	s_add_u32 m0, s40, 0x4000
	ds_read_b128 v[190:193], v241 offset:1536
	v_mfma_scale_f32_16x16x128_f8f6f4 v[28:31], v[132:135], v[178:183], v[28:31], v209, v219 op_sel_hi:[0,0,0] cbsz:4 blgp:2
	buffer_load_dwordx4 v221, s[4:7], s37 offen lds
	v_mfma_scale_f32_16x16x128_f8f6f4 v[12:15], v[128:131], v[178:183], v[12:15], v208, v219 op_sel_hi:[0,0,0] cbsz:4 blgp:2
	s_add_u32 m0, s40, 0x6000
	ds_read_b64 v[194:195], v242 offset:1536
	v_mfma_scale_f32_16x16x128_f8f6f4 v[44:47], v[136:139], v[178:183], v[44:47], v210, v219 op_sel_hi:[0,0,0] cbsz:4 blgp:2
	buffer_load_dwordx4 v225, s[4:7], s37 offen lds
	v_mfma_scale_f32_16x16x128_f8f6f4 v[60:63], v[140:143], v[178:183], v[60:63], v211, v219 op_sel_hi:[0,0,0] cbsz:4 blgp:2
	s_add_u32 m0, s40, 0x8000
	ds_read_b128 v[196:199], v241 offset:3072
	v_mfma_scale_f32_16x16x128_f8f6f4 v[56:59], v[140:143], v[172:177], v[56:59], v211, v218 op_sel_hi:[0,0,0] cbsz:4 blgp:2
	buffer_load_dwordx4 v226, s[4:7], s37 offen lds
	v_mfma_scale_f32_16x16x128_f8f6f4 v[40:43], v[136:139], v[172:177], v[40:43], v210, v218 op_sel_hi:[0,0,0] cbsz:4 blgp:2
	ds_read_b64 v[200:201], v242 offset:3072
	v_mfma_scale_f32_16x16x128_f8f6f4 v[36:39], v[136:139], v[166:171], v[36:39], v210, v217 op_sel_hi:[0,0,0] cbsz:4 blgp:2
	ds_read_b128 v[202:205], v241 offset:4608
	v_mfma_scale_f32_16x16x128_f8f6f4 v[52:55], v[140:143], v[166:171], v[52:55], v211, v217 op_sel_hi:[0,0,0] cbsz:4 blgp:2
	ds_read_b64 v[206:207], v242 offset:4608
	v_mfma_scale_f32_16x16x128_f8f6f4 v[48:51], v[140:143], v[160:165], v[48:51], v211, v216 op_sel_hi:[0,0,0] cbsz:4 blgp:2
	s_add_u32 s36, s36, 0x4000
	s_add_u32 s37, s37, 0x6000
	s_add_u32 s40, s40, 0xa000
	s_sub_u32 s41, s40, 0x1e000
	v_mfma_scale_f32_16x16x128_f8f6f4 v[32:35], v[136:139], v[160:165], v[32:35], v210, v216 op_sel_hi:[0,0,0] cbsz:4 blgp:2
	s_cmp_ge_u32 s40, s49
	s_cselect_b32 s40, s41, s40
	ds_read_b128 v[132:135], v240 offset:1024
	v_mfma_scale_f32_16x16x128_f8f6f4 v[64:67], v[144:147], v[160:165], v[64:67], v212, v216 op_sel_hi:[0,0,0] cbsz:4 blgp:2
	ds_read_b128 v[128:131], v240 offset:0
	v_mfma_scale_f32_16x16x128_f8f6f4 v[80:83], v[148:151], v[160:165], v[80:83], v213, v216 op_sel_hi:[0,0,0] cbsz:4 blgp:2
	ds_read_b128 v[140:143], v240 offset:3072
	v_mfma_scale_f32_16x16x128_f8f6f4 v[84:87], v[148:151], v[166:171], v[84:87], v213, v217 op_sel_hi:[0,0,0] cbsz:4 blgp:2
	ds_read_b128 v[136:139], v240 offset:2048
	v_mfma_scale_f32_16x16x128_f8f6f4 v[68:71], v[144:147], v[166:171], v[68:71], v212, v217 op_sel_hi:[0,0,0] cbsz:4 blgp:2
	v_mfma_scale_f32_16x16x128_f8f6f4 v[72:75], v[144:147], v[172:177], v[72:75], v212, v218 op_sel_hi:[0,0,0] cbsz:4 blgp:2
	v_mfma_scale_f32_16x16x128_f8f6f4 v[88:91], v[148:151], v[172:177], v[88:91], v213, v218 op_sel_hi:[0,0,0] cbsz:4 blgp:2
	v_mfma_scale_f32_16x16x128_f8f6f4 v[92:95], v[148:151], v[178:183], v[92:95], v213, v219 op_sel_hi:[0,0,0] cbsz:4 blgp:2
	v_mfma_scale_f32_16x16x128_f8f6f4 v[76:79], v[144:147], v[178:183], v[76:79], v212, v219 op_sel_hi:[0,0,0] cbsz:4 blgp:2
	ds_read_b128 v[148:151], v240 offset:5120
	v_mfma_scale_f32_16x16x128_f8f6f4 v[108:111], v[152:155], v[178:183], v[108:111], v214, v219 op_sel_hi:[0,0,0] cbsz:4 blgp:2
	ds_read_b128 v[144:147], v240 offset:4096
	v_mfma_scale_f32_16x16x128_f8f6f4 v[124:127], v[156:159], v[178:183], v[124:127], v215, v219 op_sel_hi:[0,0,0] cbsz:4 blgp:2
	v_mfma_scale_f32_16x16x128_f8f6f4 v[120:123], v[156:159], v[172:177], v[120:123], v215, v218 op_sel_hi:[0,0,0] cbsz:4 blgp:2
	v_mfma_scale_f32_16x16x128_f8f6f4 v[104:107], v[152:155], v[172:177], v[104:107], v214, v218 op_sel_hi:[0,0,0] cbsz:4 blgp:2
	v_mfma_scale_f32_16x16x128_f8f6f4 v[100:103], v[152:155], v[166:171], v[100:103], v214, v217 op_sel_hi:[0,0,0] cbsz:4 blgp:2
	v_mfma_scale_f32_16x16x128_f8f6f4 v[116:119], v[156:159], v[166:171], v[116:119], v215, v217 op_sel_hi:[0,0,0] cbsz:4 blgp:2
	v_mfma_scale_f32_16x16x128_f8f6f4 v[112:115], v[156:159], v[160:165], v[112:115], v215, v216 op_sel_hi:[0,0,0] cbsz:4 blgp:2
	v_mfma_scale_f32_16x16x128_f8f6f4 v[96:99], v[152:155], v[160:165], v[96:99], v214, v216 op_sel_hi:[0,0,0] cbsz:4 blgp:2
	s_add_u32 s34, s34, 1
	s_waitcnt vmcnt(5)
	s_waitcnt lgkmcnt(0)
	s_barrier
	s_mul_i32 s35, s33, 0xa000
	v_add_u32_e32 v240, s35, v222
	v_add_u32_e32 v241, s35, v223
	v_add_u32_e32 v242, s35, v224
	s_add_u32 s33, s33, 1
	s_cmp_eq_u32 s33, 3
	s_cselect_b32 s33, 0, s33
	ds_read_b128 v[152:155], v240 offset:6144
	ds_read_b128 v[156:159], v240 offset:7168
	v_mfma_scale_f32_16x16x128_f8f6f4 v[0:3], v[128:131], v[184:189], v[0:3], v208, v216 op_sel_hi:[0,0,0] cbsz:4 blgp:2
	s_cmp_eq_u32 s34, 13
	s_cselect_b32 s36, s38, s36
	s_cselect_b32 s37, s39, s37
	s_mov_b32 m0, s40
	v_mfma_scale_f32_16x16x128_f8f6f4 v[16:19], v[132:135], v[184:189], v[16:19], v209, v216 op_sel_hi:[0,0,0] cbsz:4 blgp:2
	ds_read_b128 v[160:163], v241 offset:0
	v_mfma_scale_f32_16x16x128_f8f6f4 v[20:23], v[132:135], v[190:195], v[20:23], v209, v217 op_sel_hi:[0,0,0] cbsz:4 blgp:2
	buffer_load_dwordx4 v221, s[4:7], s36 offen lds
	v_mfma_scale_f32_16x16x128_f8f6f4 v[4:7], v[128:131], v[190:195], v[4:7], v208, v217 op_sel_hi:[0,0,0] cbsz:4 blgp:2
	s_add_u32 m0, s40, 0x2000
	ds_read_b64 v[164:165], v242 offset:0
	v_mfma_scale_f32_16x16x128_f8f6f4 v[8:11], v[128:131], v[196:201], v[8:11], v208, v218 op_sel_hi:[0,0,0] cbsz:4 blgp:2
	buffer_load_dwordx4 v225, s[4:7], s36 offen lds
	v_mfma_scale_f32_16x16x128_f8f6f4 v[24:27], v[132:135], v[196:201], v[24:27], v209, v218 op_sel_hi:[0,0,0] cbsz:4 blgp:2
	s_add_u32 m0, s40, 0x4000
	ds_read_b128 v[166:169], v241 offset:1536
	v_mfma_scale_f32_16x16x128_f8f6f4 v[28:31], v[132:135], v[202:207], v[28:31], v209, v219 op_sel_hi:[0,0,0] cbsz:4 blgp:2
	buffer_load_dwordx4 v221, s[4:7], s37 offen lds
	v_mfma_scale_f32_16x16x128_f8f6f4 v[12:15], v[128:131], v[202:207], v[12:15], v208, v219 op_sel_hi:[0,0,0] cbsz:4 blgp:2
	s_add_u32 m0, s40, 0x6000
	ds_read_b64 v[170:171], v242 offset:1536
	v_mfma_scale_f32_16x16x128_f8f6f4 v[44:47], v[136:139], v[202:207], v[44:47], v210, v219 op_sel_hi:[0,0,0] cbsz:4 blgp:2
	buffer_load_dwordx4 v225, s[4:7], s37 offen lds
	v_mfma_scale_f32_16x16x128_f8f6f4 v[60:63], v[140:143], v[202:207], v[60:63], v211, v219 op_sel_hi:[0,0,0] cbsz:4 blgp:2
	s_add_u32 m0, s40, 0x8000
	ds_read_b128 v[172:175], v241 offset:3072
	v_mfma_scale_f32_16x16x128_f8f6f4 v[56:59], v[140:143], v[196:201], v[56:59], v211, v218 op_sel_hi:[0,0,0] cbsz:4 blgp:2
	buffer_load_dwordx4 v226, s[4:7], s37 offen lds
	v_mfma_scale_f32_16x16x128_f8f6f4 v[40:43], v[136:139], v[196:201], v[40:43], v210, v218 op_sel_hi:[0,0,0] cbsz:4 blgp:2
	ds_read_b64 v[176:177], v242 offset:3072
	v_mfma_scale_f32_16x16x128_f8f6f4 v[36:39], v[136:139], v[190:195], v[36:39], v210, v217 op_sel_hi:[0,0,0] cbsz:4 blgp:2
	ds_read_b128 v[178:181], v241 offset:4608
	v_mfma_scale_f32_16x16x128_f8f6f4 v[52:55], v[140:143], v[190:195], v[52:55], v211, v217 op_sel_hi:[0,0,0] cbsz:4 blgp:2
	ds_read_b64 v[182:183], v242 offset:4608
	v_mfma_scale_f32_16x16x128_f8f6f4 v[48:51], v[140:143], v[184:189], v[48:51], v211, v216 op_sel_hi:[0,0,0] cbsz:4 blgp:2
	s_add_u32 s36, s36, 0x4000
	s_add_u32 s37, s37, 0x6000
	s_add_u32 s40, s40, 0xa000
	s_sub_u32 s41, s40, 0x1e000
	v_mfma_scale_f32_16x16x128_f8f6f4 v[32:35], v[136:139], v[184:189], v[32:35], v210, v216 op_sel_hi:[0,0,0] cbsz:4 blgp:2
	s_cmp_ge_u32 s40, s49
	s_cselect_b32 s40, s41, s40
	ds_read_b128 v[132:135], v240 offset:1024
	v_mfma_scale_f32_16x16x128_f8f6f4 v[64:67], v[144:147], v[184:189], v[64:67], v212, v216 op_sel_hi:[0,0,0] cbsz:4 blgp:2
	ds_read_b128 v[128:131], v240 offset:0
	v_mfma_scale_f32_16x16x128_f8f6f4 v[80:83], v[148:151], v[184:189], v[80:83], v213, v216 op_sel_hi:[0,0,0] cbsz:4 blgp:2
	ds_read_b128 v[140:143], v240 offset:3072
	v_mfma_scale_f32_16x16x128_f8f6f4 v[84:87], v[148:151], v[190:195], v[84:87], v213, v217 op_sel_hi:[0,0,0] cbsz:4 blgp:2
	ds_read_b128 v[136:139], v240 offset:2048
	v_mfma_scale_f32_16x16x128_f8f6f4 v[68:71], v[144:147], v[190:195], v[68:71], v212, v217 op_sel_hi:[0,0,0] cbsz:4 blgp:2
	v_mfma_scale_f32_16x16x128_f8f6f4 v[72:75], v[144:147], v[196:201], v[72:75], v212, v218 op_sel_hi:[0,0,0] cbsz:4 blgp:2
	v_mfma_scale_f32_16x16x128_f8f6f4 v[88:91], v[148:151], v[196:201], v[88:91], v213, v218 op_sel_hi:[0,0,0] cbsz:4 blgp:2
	v_mfma_scale_f32_16x16x128_f8f6f4 v[92:95], v[148:151], v[202:207], v[92:95], v213, v219 op_sel_hi:[0,0,0] cbsz:4 blgp:2
	v_mfma_scale_f32_16x16x128_f8f6f4 v[76:79], v[144:147], v[202:207], v[76:79], v212, v219 op_sel_hi:[0,0,0] cbsz:4 blgp:2
	ds_read_b128 v[148:151], v240 offset:5120
	v_mfma_scale_f32_16x16x128_f8f6f4 v[108:111], v[244:247], v[202:207], v[108:111], v214, v219 op_sel_hi:[0,0,0] cbsz:4 blgp:2
	ds_read_b128 v[144:147], v240 offset:4096
	v_mfma_scale_f32_16x16x128_f8f6f4 v[124:127], v[252:255], v[202:207], v[124:127], v215, v219 op_sel_hi:[0,0,0] cbsz:4 blgp:2
	v_mfma_scale_f32_16x16x128_f8f6f4 v[120:123], v[252:255], v[196:201], v[120:123], v215, v218 op_sel_hi:[0,0,0] cbsz:4 blgp:2
	v_mfma_scale_f32_16x16x128_f8f6f4 v[104:107], v[244:247], v[196:201], v[104:107], v214, v218 op_sel_hi:[0,0,0] cbsz:4 blgp:2
	v_mfma_scale_f32_16x16x128_f8f6f4 v[100:103], v[244:247], v[190:195], v[100:103], v214, v217 op_sel_hi:[0,0,0] cbsz:4 blgp:2
	v_mfma_scale_f32_16x16x128_f8f6f4 v[116:119], v[252:255], v[190:195], v[116:119], v215, v217 op_sel_hi:[0,0,0] cbsz:4 blgp:2
	v_mfma_scale_f32_16x16x128_f8f6f4 v[112:115], v[252:255], v[184:189], v[112:115], v215, v216 op_sel_hi:[0,0,0] cbsz:4 blgp:2
	v_mfma_scale_f32_16x16x128_f8f6f4 v[96:99], v[244:247], v[184:189], v[96:99], v214, v216 op_sel_hi:[0,0,0] cbsz:4 blgp:2
	s_cmp_eq_u32 s34, 13
	s_cbranch_scc0 .Lnosc_or0
	s_add_u32 s44, s23, 1
	s_and_b32 s44, s44, 1
	s_cmp_lt_u32 s18, 4
	s_cselect_b32 s80, s26, s27
	s_cselect_b32 s82, s8, s10
	s_cselect_b32 s83, s9, s11
	s_lshl_b32 s80, s80, 10
	s_and_b32 s84, s18, 3
	s_lshl_b32 s84, s84, 8
	s_add_u32 s80, s80, s84
	s_add_u32 s82, s82, s80
	s_addc_u32 s83, s83, 0
	s_lshl_b32 s84, s44, 11
	s_lshl_b32 s85, s18, 8
	s_add_u32 s84, s84, s85
	s_add_u32 s84, s84, 0x1e000
	s_mov_b32 m0, s84
	v_lshlrev_b32_e32 v236, 2, v220
	global_load_lds_dword v236, s[82:83]
